# grid barrier: the L1 invalidate is issued right after the arrival atomic (overlaps the L2 write-back / the release poll) instead of after the release is observed; no loads are issued by the CU in betw
# speedup vs baseline: 1.0156x; 1.0156x over previous
; __device__ __forceinline__ unsigned xb_ld(unsigned* p)              { return __hip_atomic_load(p, __ATOMIC_RELAXED, __HIP_MEMORY_SCOPE_AGENT); }
; __device__ __forceinline__ unsigned xb_add(unsigned* p, unsigned v) { return __hip_atomic_fetch_add(p, v, __ATOMIC_RELAXED, __HIP_MEMORY_SCOPE_AGENT); }
; #define XB_SPIN(cond, bar) do { unsigned _sp = 0; while (cond) { __builtin_amdgcn_s_sleep(1); \
;     if ((++_sp & 255u) == 0u) { if (xb_ld(&(bar)[XB_TMO])) break; if (_sp > XB_SPIN_CAP) { atomicAdd(&(bar)[XB_TMO], 1u); break; } } } } while (0)
; __device__ __forceinline__ void xcd_barrier(const XcdBarrier& b) {
;     ...
;         const unsigned old = xb_add(&bar[XB_XSUB(b.x)], 1u);
;         const unsigned gen = old / nloc;
;         if (old + 1u == (gen + 1u) * nloc) {
;             __builtin_amdgcn_fence(__ATOMIC_RELEASE, "agent");
;             asm volatile("s_waitcnt vmcnt(0)" ::: "memory");
;             const unsigned og = xb_add(&bar[XB_TOP], 1u);
;             const unsigned tg = og / nx;
;             if (og + 1u == (tg + 1u) * nx) xb_add(&bar[XB_TOPGEN], 1u);
;             else XB_SPIN(xb_ld(&bar[XB_TOPGEN]) == tg, bar);
;             __builtin_amdgcn_fence(__ATOMIC_ACQUIRE, "agent");
;             xb_add(&bar[XB_XGEN(b.x)], 1u);
;             asm volatile("s_waitcnt vmcnt(0)" ::: "memory");
;         } else {
;             XB_SPIN(xb_ld(&bar[XB_XGEN(b.x)]) == gen, bar);
.LBB0_150:
	s_mov_b64 s[8:9], exec
	v_readlane_b32 s3, v254, 26
	s_lshl_b32 s6, s3, 8
	v_readlane_b32 s10, v254, 24
	v_mbcnt_lo_u32_b32 v2, s8, 0
	v_readlane_b32 s11, v254, 25
	s_add_u32 s6, s10, s6
	v_mbcnt_hi_u32_b32 v2, s9, v2
	s_addc_u32 s7, s11, 0
	v_cmp_eq_u32_e32 vcc, 0, v2
	s_and_saveexec_b64 s[10:11], vcc
	s_cbranch_execz .LBB0_152
	s_bcnt1_i32_b64 s8, s[8:9]
	v_mov_b32_e32 v4, 0x1000
	v_mov_b32_e32 v5, s8
	global_atomic_add v4, v4, v5, s[6:7] offset:1024 sc0
	buffer_inv sc1
.LBB0_152:
	s_or_b64 exec, exec, s[10:11]
	v_cvt_f32_u32_e32 v5, v3
	s_waitcnt vmcnt(1)
	v_readfirstlane_b32 s8, v4
	v_sub_u32_e32 v4, 0, v3
	v_rcp_iflag_f32_e32 v5, v5
	v_add_u32_e32 v6, s8, v2
	v_mul_f32_e32 v5, 0x4f7ffffe, v5
	v_cvt_u32_f32_e32 v5, v5
	v_mul_lo_u32 v2, v4, v5
	v_mul_hi_u32 v2, v5, v2
	v_add_u32_e32 v2, v5, v2
	v_mul_hi_u32 v2, v6, v2
	v_mul_lo_u32 v4, v2, v3
	v_sub_u32_e32 v4, v6, v4
	v_add_u32_e32 v5, 1, v2
	v_cmp_ge_u32_e32 vcc, v4, v3
	s_nop 1
	v_cndmask_b32_e32 v2, v2, v5, vcc
	v_sub_u32_e32 v5, v4, v3
	v_cndmask_b32_e32 v4, v4, v5, vcc
	v_add_u32_e32 v5, 1, v2
	v_cmp_ge_u32_e32 vcc, v4, v3
	v_add_u32_e32 v4, 1, v6
	s_nop 0
	v_cndmask_b32_e32 v2, v2, v5, vcc
	v_mul_lo_u32 v5, v3, v2
	v_add_u32_e32 v3, v5, v3
	v_cmp_ne_u32_e32 vcc, v4, v3
	s_and_saveexec_b64 s[8:9], vcc
	s_xor_b64 s[8:9], exec, s[8:9]
	s_cbranch_execz .LBB0_166
	s_waitcnt lgkmcnt(0)
	v_mov_b32_e32 v1, 0x2000
	global_load_dword v1, v1, s[6:7] offset:1024 sc1
	s_add_u32 s14, s6, 0x2400
	s_addc_u32 s15, s7, 0
	s_waitcnt vmcnt(0)
	v_cmp_eq_u32_e32 vcc, v1, v2
	s_and_saveexec_b64 s[10:11], vcc
	s_cbranch_execz .LBB0_165
	s_add_u32 s12, s88, 0x4200
	s_addc_u32 s13, s89, 0
	s_mov_b32 s28, 1
	s_mov_b64 s[16:17], 0
	v_mov_b32_e32 v1, 0
	s_branch .LBB0_156

; __device__ __forceinline__ unsigned xb_ld(unsigned* p)              { return __hip_atomic_load(p, __ATOMIC_RELAXED, __HIP_MEMORY_SCOPE_AGENT); }
; #define XB_SPIN(cond, bar) do { unsigned _sp = 0; while (cond) { __builtin_amdgcn_s_sleep(1); \
;     if ((++_sp & 255u) == 0u) { if (xb_ld(&(bar)[XB_TMO])) break; if (_sp > XB_SPIN_CAP) { atomicAdd(&(bar)[XB_TMO], 1u); break; } } } } while (0)
; __device__ __forceinline__ void xcd_barrier(const XcdBarrier& b) {
;     ...
;             XB_SPIN(xb_ld(&bar[XB_XGEN(b.x)]) == gen, bar);
;             __builtin_amdgcn_fence(__ATOMIC_ACQUIRE, "agent");
;             asm volatile("s_waitcnt vmcnt(0)" ::: "memory");
.LBB0_165:
	s_or_b64 exec, exec, s[10:11]
	s_waitcnt vmcnt(0)
	s_waitcnt vmcnt(0)

; __device__ __forceinline__ unsigned xb_add(unsigned* p, unsigned v) { return __hip_atomic_fetch_add(p, v, __ATOMIC_RELAXED, __HIP_MEMORY_SCOPE_AGENT); }
; __device__ __forceinline__ void xcd_barrier(const XcdBarrier& b) {
;     ...
;             __builtin_amdgcn_fence(__ATOMIC_ACQUIRE, "agent");
;             xb_add(&bar[XB_XGEN(b.x)], 1u);
;             asm volatile("s_waitcnt vmcnt(0)" ::: "memory");
.LBB0_183:
	s_or_b64 exec, exec, s[8:9]
	s_mov_b64 s[8:9], exec
	v_mbcnt_lo_u32_b32 v1, s8, 0
	v_mbcnt_hi_u32_b32 v1, s9, v1
	v_cmp_eq_u32_e32 vcc, 0, v1
	s_waitcnt vmcnt(0)
	s_and_saveexec_b64 s[10:11], vcc
	s_cbranch_execz .LBB0_185
	s_bcnt1_i32_b64 s8, s[8:9]
	v_mov_b32_e32 v1, 0x2000
	v_mov_b32_e32 v2, s8
	global_atomic_add v1, v2, s[6:7] offset:1024

; __device__ __forceinline__ unsigned xb_add(unsigned* p, unsigned v) { return __hip_atomic_fetch_add(p, v, __ATOMIC_RELAXED, __HIP_MEMORY_SCOPE_AGENT); }
; __device__ __forceinline__ void xcd_barrier(const XcdBarrier& b) {
;     ...
;         const unsigned old = xb_add(&bar[XB_XSUB(b.x)], 1u);
.LBB0_1603:
	s_mov_b64 s[8:9], exec
	v_readlane_b32 s6, v254, 26
	s_lshl_b32 s6, s6, 8
	v_readlane_b32 s10, v254, 24
	v_mbcnt_lo_u32_b32 v2, s8, 0
	v_readlane_b32 s11, v254, 25
	s_add_u32 s6, s10, s6
	v_mbcnt_hi_u32_b32 v2, s9, v2
	s_addc_u32 s7, s11, 0
	v_cmp_eq_u32_e32 vcc, 0, v2
	s_and_saveexec_b64 s[10:11], vcc
	s_cbranch_execz .LBB0_1605
	s_bcnt1_i32_b64 s8, s[8:9]
	v_mov_b32_e32 v4, 0x1000
	v_mov_b32_e32 v5, s8
	global_atomic_add v4, v4, v5, s[6:7] offset:1024 sc0
	buffer_inv sc1

; __device__ __forceinline__ unsigned xb_ld(unsigned* p)              { return __hip_atomic_load(p, __ATOMIC_RELAXED, __HIP_MEMORY_SCOPE_AGENT); }
; __device__ __forceinline__ unsigned xb_add(unsigned* p, unsigned v) { return __hip_atomic_fetch_add(p, v, __ATOMIC_RELAXED, __HIP_MEMORY_SCOPE_AGENT); }
; #define XB_SPIN(cond, bar) do { unsigned _sp = 0; while (cond) { __builtin_amdgcn_s_sleep(1); \
;     if ((++_sp & 255u) == 0u) { if (xb_ld(&(bar)[XB_TMO])) break; if (_sp > XB_SPIN_CAP) { atomicAdd(&(bar)[XB_TMO], 1u); break; } } } } while (0)
; __device__ __forceinline__ void xcd_barrier(const XcdBarrier& b) {
;     ...
;         const unsigned old = xb_add(&bar[XB_XSUB(b.x)], 1u);
;         const unsigned gen = old / nloc;
;         if (old + 1u == (gen + 1u) * nloc) {
;             __builtin_amdgcn_fence(__ATOMIC_RELEASE, "agent");
;             asm volatile("s_waitcnt vmcnt(0)" ::: "memory");
;             const unsigned og = xb_add(&bar[XB_TOP], 1u);
;             const unsigned tg = og / nx;
;             if (og + 1u == (tg + 1u) * nx) xb_add(&bar[XB_TOPGEN], 1u);
;             else XB_SPIN(xb_ld(&bar[XB_TOPGEN]) == tg, bar);
;             __builtin_amdgcn_fence(__ATOMIC_ACQUIRE, "agent");
;             xb_add(&bar[XB_XGEN(b.x)], 1u);
;             asm volatile("s_waitcnt vmcnt(0)" ::: "memory");
;         } else {
;             XB_SPIN(xb_ld(&bar[XB_XGEN(b.x)]) == gen, bar);
.LBB0_1890:
	s_mov_b64 s[6:7], exec
	v_readlane_b32 s4, v254, 26
	s_lshl_b32 s4, s4, 8
	v_readlane_b32 s8, v254, 24
	v_mbcnt_lo_u32_b32 v2, s6, 0
	v_readlane_b32 s9, v254, 25
	s_add_u32 s4, s8, s4
	v_mbcnt_hi_u32_b32 v2, s7, v2
	s_addc_u32 s5, s9, 0
	v_cmp_eq_u32_e32 vcc, 0, v2
	s_and_saveexec_b64 s[8:9], vcc
	s_cbranch_execz .LBB0_1892
	s_bcnt1_i32_b64 s6, s[6:7]
	v_mov_b32_e32 v4, 0x1000
	v_mov_b32_e32 v5, s6
	global_atomic_add v4, v4, v5, s[4:5] offset:1024 sc0
	buffer_inv sc1
.LBB0_1892:
	s_or_b64 exec, exec, s[8:9]
	v_cvt_f32_u32_e32 v5, v3
	s_waitcnt vmcnt(1)
	v_readfirstlane_b32 s6, v4
	v_sub_u32_e32 v4, 0, v3
	v_rcp_iflag_f32_e32 v5, v5
	v_add_u32_e32 v6, s6, v2
	v_mul_f32_e32 v5, 0x4f7ffffe, v5
	v_cvt_u32_f32_e32 v5, v5
	v_mul_lo_u32 v2, v4, v5
	v_mul_hi_u32 v2, v5, v2
	v_add_u32_e32 v2, v5, v2
	v_mul_hi_u32 v2, v6, v2
	v_mul_lo_u32 v4, v2, v3
	v_sub_u32_e32 v4, v6, v4
	v_add_u32_e32 v5, 1, v2
	v_cmp_ge_u32_e32 vcc, v4, v3
	s_nop 1
	v_cndmask_b32_e32 v2, v2, v5, vcc
	v_sub_u32_e32 v5, v4, v3
	v_cndmask_b32_e32 v4, v4, v5, vcc
	v_add_u32_e32 v5, 1, v2
	v_cmp_ge_u32_e32 vcc, v4, v3
	v_add_u32_e32 v4, 1, v6
	s_nop 0
	v_cndmask_b32_e32 v2, v2, v5, vcc
	v_mul_lo_u32 v5, v3, v2
	v_add_u32_e32 v3, v5, v3
	v_cmp_ne_u32_e32 vcc, v4, v3
	s_and_saveexec_b64 s[6:7], vcc
	s_xor_b64 s[6:7], exec, s[6:7]
	s_cbranch_execz .LBB0_1906
	s_waitcnt lgkmcnt(0)
	v_mov_b32_e32 v1, 0x2000
	global_load_dword v1, v1, s[4:5] offset:1024 sc1
	s_add_u32 s12, s4, 0x2400
	s_addc_u32 s13, s5, 0
	s_waitcnt vmcnt(0)
	v_cmp_eq_u32_e32 vcc, v1, v2
	s_and_saveexec_b64 s[8:9], vcc
	s_cbranch_execz .LBB0_1905
	s_add_u32 s10, s88, 0x4200
	s_addc_u32 s11, s89, 0
	s_mov_b32 s26, 1
	s_mov_b64 s[14:15], 0
	v_mov_b32_e32 v1, 0
	s_branch .LBB0_1896

; __device__ __forceinline__ unsigned xb_ld(unsigned* p)              { return __hip_atomic_load(p, __ATOMIC_RELAXED, __HIP_MEMORY_SCOPE_AGENT); }
; #define XB_SPIN(cond, bar) do { unsigned _sp = 0; while (cond) { __builtin_amdgcn_s_sleep(1); \
;     if ((++_sp & 255u) == 0u) { if (xb_ld(&(bar)[XB_TMO])) break; if (_sp > XB_SPIN_CAP) { atomicAdd(&(bar)[XB_TMO], 1u); break; } } } } while (0)
; __device__ __forceinline__ void xcd_barrier(const XcdBarrier& b) {
;     ...
;             XB_SPIN(xb_ld(&bar[XB_XGEN(b.x)]) == gen, bar);
;             __builtin_amdgcn_fence(__ATOMIC_ACQUIRE, "agent");
;             asm volatile("s_waitcnt vmcnt(0)" ::: "memory");
.LBB0_1905:
	s_or_b64 exec, exec, s[8:9]
	s_waitcnt vmcnt(0)
	s_waitcnt vmcnt(0)

; __device__ __forceinline__ unsigned xb_add(unsigned* p, unsigned v) { return __hip_atomic_fetch_add(p, v, __ATOMIC_RELAXED, __HIP_MEMORY_SCOPE_AGENT); }
; __device__ __forceinline__ void xcd_barrier(const XcdBarrier& b) {
;     ...
;             __builtin_amdgcn_fence(__ATOMIC_ACQUIRE, "agent");
;             xb_add(&bar[XB_XGEN(b.x)], 1u);
;             asm volatile("s_waitcnt vmcnt(0)" ::: "memory");
.LBB0_1923:
	s_or_b64 exec, exec, s[6:7]
	s_mov_b64 s[6:7], exec
	v_mbcnt_lo_u32_b32 v1, s6, 0
	v_mbcnt_hi_u32_b32 v1, s7, v1
	v_cmp_eq_u32_e32 vcc, 0, v1
	s_waitcnt vmcnt(0)
	s_and_saveexec_b64 s[8:9], vcc
	s_cbranch_execz .LBB0_1925
	s_bcnt1_i32_b64 s6, s[6:7]
	v_mov_b32_e32 v1, 0x2000
	v_mov_b32_e32 v2, s6
	global_atomic_add v1, v2, s[4:5] offset:1024

; __device__ __forceinline__ unsigned xb_add(unsigned* p, unsigned v) { return __hip_atomic_fetch_add(p, v, __ATOMIC_RELAXED, __HIP_MEMORY_SCOPE_AGENT); }
; __device__ __forceinline__ void xcd_barrier(const XcdBarrier& b) {
;     ...
;         const unsigned old = xb_add(&bar[XB_XSUB(b.x)], 1u);
.LBB0_3593:
	s_mov_b64 s[6:7], exec
	v_readlane_b32 s3, v254, 26
	s_lshl_b32 s4, s3, 8
	v_readlane_b32 s8, v254, 24
	v_mbcnt_lo_u32_b32 v2, s6, 0
	v_readlane_b32 s9, v254, 25
	s_add_u32 s4, s8, s4
	v_mbcnt_hi_u32_b32 v2, s7, v2
	s_addc_u32 s5, s9, 0
	v_cmp_eq_u32_e32 vcc, 0, v2
	s_and_saveexec_b64 s[8:9], vcc
	s_cbranch_execz .LBB0_3595
	s_bcnt1_i32_b64 s6, s[6:7]
	v_mov_b32_e32 v4, 0x1000
	v_mov_b32_e32 v5, s6
	global_atomic_add v4, v4, v5, s[4:5] offset:1024 sc0
	buffer_inv sc1

; __device__ __forceinline__ unsigned xb_ld(unsigned* p)              { return __hip_atomic_load(p, __ATOMIC_RELAXED, __HIP_MEMORY_SCOPE_AGENT); }
; __device__ __forceinline__ unsigned xb_add(unsigned* p, unsigned v) { return __hip_atomic_fetch_add(p, v, __ATOMIC_RELAXED, __HIP_MEMORY_SCOPE_AGENT); }
; #define XB_SPIN(cond, bar) do { unsigned _sp = 0; while (cond) { __builtin_amdgcn_s_sleep(1); \
;     if ((++_sp & 255u) == 0u) { if (xb_ld(&(bar)[XB_TMO])) break; if (_sp > XB_SPIN_CAP) { atomicAdd(&(bar)[XB_TMO], 1u); break; } } } } while (0)
; __device__ __forceinline__ void xcd_barrier(const XcdBarrier& b) {
;     ...
;         const unsigned old = xb_add(&bar[XB_XSUB(b.x)], 1u);
;         const unsigned gen = old / nloc;
;         if (old + 1u == (gen + 1u) * nloc) {
;             __builtin_amdgcn_fence(__ATOMIC_RELEASE, "agent");
;             asm volatile("s_waitcnt vmcnt(0)" ::: "memory");
;             const unsigned og = xb_add(&bar[XB_TOP], 1u);
;             const unsigned tg = og / nx;
;             if (og + 1u == (tg + 1u) * nx) xb_add(&bar[XB_TOPGEN], 1u);
;             else XB_SPIN(xb_ld(&bar[XB_TOPGEN]) == tg, bar);
;             __builtin_amdgcn_fence(__ATOMIC_ACQUIRE, "agent");
;             xb_add(&bar[XB_XGEN(b.x)], 1u);
;             asm volatile("s_waitcnt vmcnt(0)" ::: "memory");
;         } else {
;             XB_SPIN(xb_ld(&bar[XB_XGEN(b.x)]) == gen, bar);
.LBB0_3786:
	s_mov_b64 s[10:11], exec
	v_readlane_b32 s3, v254, 26
	s_lshl_b32 s3, s3, 8
	v_readlane_b32 s6, v254, 24
	v_mbcnt_lo_u32_b32 v2, s10, 0
	v_readlane_b32 s7, v254, 25
	s_add_u32 s6, s6, s3
	v_mbcnt_hi_u32_b32 v2, s11, v2
	s_addc_u32 s7, s7, 0
	v_cmp_eq_u32_e32 vcc, 0, v2
	s_and_saveexec_b64 s[12:13], vcc
	s_cbranch_execz .LBB0_3788
	s_bcnt1_i32_b64 s3, s[10:11]
	v_mov_b32_e32 v4, 0x1000
	v_mov_b32_e32 v5, s3
	global_atomic_add v4, v4, v5, s[6:7] offset:1024 sc0
	buffer_inv sc1
.LBB0_3788:
	s_or_b64 exec, exec, s[12:13]
	v_cvt_f32_u32_e32 v5, v3
	s_waitcnt vmcnt(1)
	v_readfirstlane_b32 s3, v4
	v_sub_u32_e32 v4, 0, v3
	v_rcp_iflag_f32_e32 v5, v5
	v_add_u32_e32 v6, s3, v2
	v_mul_f32_e32 v5, 0x4f7ffffe, v5
	v_cvt_u32_f32_e32 v5, v5
	v_mul_lo_u32 v2, v4, v5
	v_mul_hi_u32 v2, v5, v2
	v_add_u32_e32 v2, v5, v2
	v_mul_hi_u32 v2, v6, v2
	v_mul_lo_u32 v4, v2, v3
	v_sub_u32_e32 v4, v6, v4
	v_add_u32_e32 v5, 1, v2
	v_cmp_ge_u32_e32 vcc, v4, v3
	s_nop 1
	v_cndmask_b32_e32 v2, v2, v5, vcc
	v_sub_u32_e32 v5, v4, v3
	v_cndmask_b32_e32 v4, v4, v5, vcc
	v_add_u32_e32 v5, 1, v2
	v_cmp_ge_u32_e32 vcc, v4, v3
	v_add_u32_e32 v4, 1, v6
	s_nop 0
	v_cndmask_b32_e32 v2, v2, v5, vcc
	v_mul_lo_u32 v5, v3, v2
	v_add_u32_e32 v3, v5, v3
	v_cmp_ne_u32_e32 vcc, v4, v3
	s_and_saveexec_b64 s[10:11], vcc
	s_xor_b64 s[10:11], exec, s[10:11]
	s_cbranch_execz .LBB0_3802
	s_waitcnt lgkmcnt(0)
	v_mov_b32_e32 v1, 0x2000
	global_load_dword v1, v1, s[6:7] offset:1024 sc1
	s_add_u32 s16, s6, 0x2400
	s_addc_u32 s17, s7, 0
	s_waitcnt vmcnt(0)
	v_cmp_eq_u32_e32 vcc, v1, v2
	s_and_saveexec_b64 s[12:13], vcc
	s_cbranch_execz .LBB0_3801
	s_add_u32 s14, s88, 0x4200
	s_addc_u32 s15, s89, 0
	s_mov_b32 s3, 1
	s_mov_b64 s[20:21], 0
	v_mov_b32_e32 v1, 0
	s_branch .LBB0_3792

; __device__ __forceinline__ unsigned xb_ld(unsigned* p)              { return __hip_atomic_load(p, __ATOMIC_RELAXED, __HIP_MEMORY_SCOPE_AGENT); }
; #define XB_SPIN(cond, bar) do { unsigned _sp = 0; while (cond) { __builtin_amdgcn_s_sleep(1); \
;     if ((++_sp & 255u) == 0u) { if (xb_ld(&(bar)[XB_TMO])) break; if (_sp > XB_SPIN_CAP) { atomicAdd(&(bar)[XB_TMO], 1u); break; } } } } while (0)
; __device__ __forceinline__ void xcd_barrier(const XcdBarrier& b) {
;     ...
;             XB_SPIN(xb_ld(&bar[XB_XGEN(b.x)]) == gen, bar);
;             __builtin_amdgcn_fence(__ATOMIC_ACQUIRE, "agent");
;             asm volatile("s_waitcnt vmcnt(0)" ::: "memory");
.LBB0_3801:
	s_or_b64 exec, exec, s[12:13]
	s_waitcnt vmcnt(0)
	s_waitcnt vmcnt(0)

; __device__ __forceinline__ unsigned xb_add(unsigned* p, unsigned v) { return __hip_atomic_fetch_add(p, v, __ATOMIC_RELAXED, __HIP_MEMORY_SCOPE_AGENT); }
; __device__ __forceinline__ void xcd_barrier(const XcdBarrier& b) {
;     ...
;             __builtin_amdgcn_fence(__ATOMIC_ACQUIRE, "agent");
;             xb_add(&bar[XB_XGEN(b.x)], 1u);
;             asm volatile("s_waitcnt vmcnt(0)" ::: "memory");
.LBB0_3819:
	s_or_b64 exec, exec, s[10:11]
	s_mov_b64 s[10:11], exec
	v_mbcnt_lo_u32_b32 v1, s10, 0
	v_mbcnt_hi_u32_b32 v1, s11, v1
	v_cmp_eq_u32_e32 vcc, 0, v1
	s_waitcnt vmcnt(0)
	s_and_saveexec_b64 s[12:13], vcc
	s_cbranch_execz .LBB0_3821
	s_bcnt1_i32_b64 s3, s[10:11]
	v_mov_b32_e32 v1, 0x2000
	v_mov_b32_e32 v2, s3
	global_atomic_add v1, v2, s[6:7] offset:1024
